# p1 gather: the eight row-pointer slot fetches of a pass issued together with one wait (was eight dependent LDS round trips)
# baseline (speedup 1.0000x reference)
; __device__ __forceinline__ int shl_from_i(int v, int src_lane) { return __builtin_amdgcn_ds_bpermute(src_lane << 2, v); }
; __device__ __forceinline__ void p1_gather_issue(u32x2 (&wa)[4][4], u32x2 (&wb)[4][4], unsigned& maska, unsigned& maskb, int inva, int invb, const bf16_t* Yp, const bf16_t* zrow, int lane) {
;     maska = (unsigned)__ballot(inva >= 0) & 0xffffu; maskb = (unsigned)__ballot(invb >= 0) & 0xffffu;
;     const bf16_t* ypa[4]; const bf16_t* ypb[4];
; #pragma unroll
;     for (int q = 0; q < 4; ++q) {
;         if (maska) { const int e = __builtin_ctz(maska); maska &= maska - 1; ypa[q] = Yp + (size_t)shl_from_i(inva, e) * D; } else ypa[q] = zrow;
;         if (maskb) { const int e = __builtin_ctz(maskb); maskb &= maskb - 1; ypb[q] = Yp + (size_t)shl_from_i(invb, e) * D; } else ypb[q] = zrow; }
; #pragma unroll
;     for (int q = 0; q < 4; ++q)
; #pragma unroll
;         for (int j = 0; j < 4; ++j) { wa[q][j] = *(const u32x2*)(ypa[q] + 4 * (lane + 64 * j)); wb[q][j] = *(const u32x2*)(ypb[q] + 4 * (lane + 64 * j)); }
; }
; __device__ __forceinline__ void p1_gather_consume(f32x4 (&va)[4], f32x4 (&vb)[4], u32x2 (&wa)[4][4], u32x2 (&wb)[4][4], unsigned maska, unsigned maskb, int inva, int invb,
;                                                   const bf16_t* Yp, const bf16_t* zrow, const f32x4 (&g2)[4], int lane) {
;     f32x4 aa[4], ab[4];
; #pragma unroll
;     for (int j = 0; j < 4; ++j) { aa[j] = (f32x4){0.f, 0.f, 0.f, 0.f}; ab[j] = (f32x4){0.f, 0.f, 0.f, 0.f}; }
.LBB0_166:
	s_and_b64 vcc, exec, s[40:41]
	s_or_b32 s62, s6, 1
	s_cbranch_vccnz .LBB0_205
	v_cmp_lt_i32_e64 s[4:5], -1, v245
	v_cmp_lt_i32_e64 s[2:3], -1, v244
	s_and_b32 s6, s4, 0xffff
	s_and_b32 s4, s2, 0xffff
	s_ff1_i32_b32 s88, s6
	s_add_i32 s5, s6, -1
	s_and_b32 s5, s5, s6
	s_lshl_b32 s88, s88, 2
	s_ff1_i32_b32 s90, s5
	s_add_i32 s7, s5, -1
	s_and_b32 s7, s7, s5
	s_lshl_b32 s90, s90, 2
	s_ff1_i32_b32 s92, s7
	s_add_i32 s96, s7, -1
	s_and_b32 s96, s96, s7
	s_lshl_b32 s92, s92, 2
	s_ff1_i32_b32 s94, s96
	s_add_i32 s3, s96, -1
	s_and_b32 s3, s3, s96
	s_lshl_b32 s94, s94, 2
	s_ff1_i32_b32 s89, s4
	s_add_i32 s97, s4, -1
	s_and_b32 s97, s97, s4
	s_lshl_b32 s89, s89, 2
	s_ff1_i32_b32 s91, s97
	s_add_i32 s98, s97, -1
	s_and_b32 s98, s98, s97
	s_lshl_b32 s91, s91, 2
	s_ff1_i32_b32 s93, s98
	s_add_i32 s99, s98, -1
	s_and_b32 s99, s99, s98
	s_lshl_b32 s93, s93, 2
	s_ff1_i32_b32 s95, s99
	s_add_i32 s2, s99, -1
	s_and_b32 s2, s2, s99
	s_lshl_b32 s95, s95, 2
	v_mov_b32_e32 v112, s88
	ds_bpermute_b32 v114, v112, v245
	v_mov_b32_e32 v113, s89
	ds_bpermute_b32 v116, v113, v244
	v_mov_b32_e32 v112, s90
	ds_bpermute_b32 v174, v112, v245
	v_mov_b32_e32 v113, s91
	ds_bpermute_b32 v168, v113, v244
	v_mov_b32_e32 v112, s92
	ds_bpermute_b32 v176, v112, v245
	v_mov_b32_e32 v113, s93
	ds_bpermute_b32 v182, v113, v244
	v_mov_b32_e32 v112, s94
	ds_bpermute_b32 v186, v112, v245
	v_mov_b32_e32 v113, s95
	ds_bpermute_b32 v188, v113, v244
	s_waitcnt lgkmcnt(0)
	s_cmp_eq_u32 s6, 0
	s_cbranch_scc1 .Lp1g_e0
	v_ashrrev_i32_e32 v115, 31, v114
	v_lshlrev_b64 v[114:115], 11, v[114:115]
	v_lshl_add_u64 v[114:115], s[52:53], 0, v[114:115]
	s_branch .Lp1g_n0
.Lp1g_e0:
	v_mov_b64_e32 v[114:115], s[54:55]
.Lp1g_n0:
	s_cmp_eq_u32 s4, 0
	s_cbranch_scc1 .Lp1g_e1
	v_ashrrev_i32_e32 v117, 31, v116
	v_lshlrev_b64 v[116:117], 11, v[116:117]
	v_lshl_add_u64 v[116:117], s[52:53], 0, v[116:117]
	s_branch .Lp1g_n1
.Lp1g_e1:
	v_mov_b64_e32 v[116:117], s[54:55]
.Lp1g_n1:
	s_cmp_eq_u32 s5, 0
	s_cbranch_scc1 .Lp1g_e2
	v_ashrrev_i32_e32 v175, 31, v174
	v_lshlrev_b64 v[174:175], 11, v[174:175]
	v_lshl_add_u64 v[174:175], s[52:53], 0, v[174:175]
	s_branch .Lp1g_n2
.Lp1g_e2:
	v_mov_b64_e32 v[174:175], s[54:55]
.Lp1g_n2:
	s_cmp_eq_u32 s97, 0
	s_cbranch_scc1 .Lp1g_e3
	v_ashrrev_i32_e32 v169, 31, v168
	v_lshlrev_b64 v[168:169], 11, v[168:169]
	v_lshl_add_u64 v[168:169], s[52:53], 0, v[168:169]
	s_branch .Lp1g_n3
.Lp1g_e3:
	v_mov_b64_e32 v[168:169], s[54:55]
.Lp1g_n3:
	s_cmp_eq_u32 s7, 0
	s_cbranch_scc1 .Lp1g_e4
	v_ashrrev_i32_e32 v177, 31, v176
	v_lshlrev_b64 v[176:177], 11, v[176:177]
	v_lshl_add_u64 v[176:177], s[52:53], 0, v[176:177]
	s_branch .Lp1g_n4
.Lp1g_e4:
	v_mov_b64_e32 v[176:177], s[54:55]
.Lp1g_n4:
	s_cmp_eq_u32 s98, 0
	s_cbranch_scc1 .Lp1g_e5
	v_ashrrev_i32_e32 v183, 31, v182
	v_lshlrev_b64 v[182:183], 11, v[182:183]
	v_lshl_add_u64 v[182:183], s[52:53], 0, v[182:183]
	s_branch .Lp1g_n5
.Lp1g_e5:
	v_mov_b64_e32 v[182:183], s[54:55]
.Lp1g_n5:
	s_cmp_eq_u32 s96, 0
	s_cbranch_scc1 .Lp1g_e6
	v_ashrrev_i32_e32 v187, 31, v186
	v_lshlrev_b64 v[186:187], 11, v[186:187]
	v_lshl_add_u64 v[186:187], s[52:53], 0, v[186:187]
	s_branch .Lp1g_n6
.Lp1g_e6:
	v_mov_b64_e32 v[186:187], s[54:55]
.Lp1g_n6:
	s_cmp_eq_u32 s99, 0
	s_cbranch_scc1 .Lp1g_e7
	v_ashrrev_i32_e32 v189, 31, v188
	v_lshlrev_b64 v[188:189], 11, v[188:189]
	v_lshl_add_u64 v[188:189], s[52:53], 0, v[188:189]
	s_branch .Lp1g_n7
.Lp1g_e7:
	v_mov_b64_e32 v[188:189], s[54:55]
.Lp1g_n7:
.LBB0_183:
	v_lshlrev_b64 v[112:113], 1, v[128:129]
	v_lshl_add_u64 v[114:115], v[114:115], 0, v[112:113]
	v_lshl_add_u64 v[116:117], v[116:117], 0, v[112:113]
	flat_load_dwordx2 v[212:213], v[114:115]
	flat_load_dwordx2 v[198:199], v[114:115] offset:512
	flat_load_dwordx2 v[184:185], v[114:115] offset:1024
	flat_load_dwordx2 v[172:173], v[114:115] offset:1536
	flat_load_dwordx2 v[208:209], v[116:117]
	flat_load_dwordx2 v[192:193], v[116:117] offset:512
	flat_load_dwordx2 v[180:181], v[116:117] offset:1024
	flat_load_dwordx2 v[170:171], v[116:117] offset:1536
	v_mov_b32_e32 v114, 0
	v_mov_b32_e32 v115, v114
	v_mov_b32_e32 v116, v114
	v_mov_b32_e32 v117, v114
	v_mov_b32_e32 v124, v114
	v_mov_b32_e32 v125, v114
	v_mov_b32_e32 v122, v114
	v_mov_b32_e32 v123, v114
	v_mov_b32_e32 v154, v114
	v_mov_b32_e32 v155, v114
	v_mov_b32_e32 v152, v114
	v_mov_b32_e32 v153, v114
	v_mov_b32_e32 v162, v114
	v_mov_b32_e32 v163, v114
	v_mov_b32_e32 v160, v114
	v_mov_b32_e32 v161, v114
	v_mov_b32_e32 v166, v114
	v_mov_b32_e32 v167, v114
	v_mov_b32_e32 v164, v114
	v_mov_b32_e32 v165, v114
	v_mov_b32_e32 v158, v114
	v_mov_b32_e32 v159, v114
	v_mov_b32_e32 v156, v114
	v_mov_b32_e32 v157, v114
	v_mov_b32_e32 v146, v114
	v_mov_b32_e32 v147, v114
	v_mov_b32_e32 v126, v114
	v_mov_b32_e32 v127, v114
	v_mov_b32_e32 v120, v114
	v_mov_b32_e32 v121, v114
	v_mov_b32_e32 v118, v114
	v_mov_b32_e32 v119, v114
	s_branch .LBB0_185
